# k_bucket_sort: row-end counters written by the scan next to the row starts (no separate LDS round trip + barrier), redundant barrier after the scatter loop removed
# speedup vs baseline: 1.0157x; 1.0097x over previous
.LBB2_50:
	s_or_b64 exec, exec, s[46:47]
	v_add_u32_e32 v85, v35, v38
	v_sub_u32_e32 v34, v35, v34
	v_lshl_or_b32 v35, s57, 9, v0
	s_mov_b32 s0, 0x186a0
	s_ashr_i32 s47, s36, 31
	s_mov_b32 s46, s36
	v_add_u32_e32 v34, v34, v38
	v_cmp_gt_i32_e64 s[0:1], s0, v35
	s_mul_i32 s48, s56, 0x186a1
	s_and_saveexec_b64 s[50:51], s[0:1]
	s_cbranch_execz .LBB2_52
	v_add_u32_e32 v38, s48, v35
	v_ashrrev_i32_e32 v39, 31, v38
	v_add_u32_e32 v37, s46, v34
	v_lshl_add_u64 v[38:39], v[38:39], 2, s[40:41]
	global_store_dword v[38:39], v37, off

.LBB2_54:
	s_or_b64 exec, exec, s[0:1]
	s_mul_hi_i32 s36, s56, 0x927c00
	s_mul_i32 s56, s56, 0x927c00
	s_cmpk_lt_i32 s33, 0x2001
	s_mov_b64 s[0:1], -1
	ds_write_b32 v36, v34
	ds_write_b32 v36, v85 offset:2112
	s_waitcnt lgkmcnt(0)
	s_barrier
	s_cbranch_scc1 .LBB2_108
	s_add_u32 s40, s42, s56
	s_addc_u32 s41, s43, s36
	s_lshl_b64 s[0:1], s[46:47], 3
	s_add_u32 s0, s40, s0
	s_addc_u32 s1, s41, s1
	s_and_saveexec_b64 s[40:41], s[30:31]
	s_cbranch_execnz .LBB2_87
	s_or_b64 exec, exec, s[40:41]
	s_and_saveexec_b64 s[40:41], s[28:29]
	s_cbranch_execnz .LBB2_88

.LBB2_108:
	s_and_b64 vcc, exec, s[0:1]
	s_cbranch_vccz .LBB2_129
	s_mov_b32 s58, 0x29f17
	v_and_b32_e32 v64, 0x1ffff, v30
	v_mul_hi_u32 v64, v64, s58
	v_cmp_lt_u32_e32 vcc, 1, v64
	v_cndmask_b32_e64 v97, 1, -1, vcc
	v_and_b32_e32 v65, 0x1ffff, v32
	v_mul_hi_u32 v65, v65, s58
	v_cmp_lt_u32_e32 vcc, 1, v65
	v_cndmask_b32_e64 v98, 1, -1, vcc
	v_and_b32_e32 v66, 0x1ffff, v18
	v_mul_hi_u32 v66, v66, s58
	v_cmp_lt_u32_e32 vcc, 1, v66
	v_cndmask_b32_e64 v99, 1, -1, vcc
	v_and_b32_e32 v67, 0x1ffff, v20
	v_mul_hi_u32 v67, v67, s58
	v_cmp_lt_u32_e32 vcc, 1, v67
	v_cndmask_b32_e64 v100, 1, -1, vcc
	v_and_b32_e32 v68, 0x1ffff, v26
	v_mul_hi_u32 v68, v68, s58
	v_cmp_lt_u32_e32 vcc, 1, v68
	v_cndmask_b32_e64 v101, 1, -1, vcc
	v_and_b32_e32 v69, 0x1ffff, v28
	v_mul_hi_u32 v69, v69, s58
	v_cmp_lt_u32_e32 vcc, 1, v69
	v_cndmask_b32_e64 v102, 1, -1, vcc
	v_and_b32_e32 v70, 0x1ffff, v10
	v_mul_hi_u32 v70, v70, s58
	v_cmp_lt_u32_e32 vcc, 1, v70
	v_cndmask_b32_e64 v103, 1, -1, vcc
	v_and_b32_e32 v71, 0x1ffff, v12
	v_mul_hi_u32 v71, v71, s58
	v_cmp_lt_u32_e32 vcc, 1, v71
	v_cndmask_b32_e64 v104, 1, -1, vcc
	v_and_b32_e32 v72, 0x1ffff, v22
	v_mul_hi_u32 v72, v72, s58
	v_cmp_lt_u32_e32 vcc, 1, v72
	v_cndmask_b32_e64 v105, 1, -1, vcc
	v_and_b32_e32 v73, 0x1ffff, v24
	v_mul_hi_u32 v73, v73, s58
	v_cmp_lt_u32_e32 vcc, 1, v73
	v_cndmask_b32_e64 v106, 1, -1, vcc
	v_and_b32_e32 v74, 0x1ffff, v6
	v_mul_hi_u32 v74, v74, s58
	v_cmp_lt_u32_e32 vcc, 1, v74
	v_cndmask_b32_e64 v107, 1, -1, vcc
	v_and_b32_e32 v75, 0x1ffff, v8
	v_mul_hi_u32 v75, v75, s58
	v_cmp_lt_u32_e32 vcc, 1, v75
	v_cndmask_b32_e64 v108, 1, -1, vcc
	v_and_b32_e32 v76, 0x1ffff, v14
	v_mul_hi_u32 v76, v76, s58
	v_cmp_lt_u32_e32 vcc, 1, v76
	v_cndmask_b32_e64 v109, 1, -1, vcc
	v_and_b32_e32 v77, 0x1ffff, v16
	v_mul_hi_u32 v77, v77, s58
	v_cmp_lt_u32_e32 vcc, 1, v77
	v_cndmask_b32_e64 v110, 1, -1, vcc
	v_and_b32_e32 v78, 0x1ffff, v2
	v_mul_hi_u32 v78, v78, s58
	v_cmp_lt_u32_e32 vcc, 1, v78
	v_cndmask_b32_e64 v111, 1, -1, vcc
	v_and_b32_e32 v79, 0x1ffff, v4
	v_mul_hi_u32 v79, v79, s58
	v_cmp_lt_u32_e32 vcc, 1, v79
	v_cndmask_b32_e64 v112, 1, -1, vcc
	s_mov_b32 s92, 0x10000
	s_mov_b32 s59, 0
	s_mov_b32 s58, 3

.LBB2_126:
	s_or_b64 exec, exec, s[0:1]
	s_sub_i32 s4, s37, s46
	v_cmp_gt_i32_e32 vcc, s4, v0
	s_and_saveexec_b64 s[0:1], vcc
	s_cbranch_execz .LBB2_129
	s_lshl_b64 s[0:1], s[46:47], 3
	s_add_u32 s0, s56, s0
	s_addc_u32 s1, s36, s1
	s_add_u32 s0, s42, s0
	v_lshlrev_b32_e32 v2, 3, v0
	v_mov_b32_e32 v3, 0
	s_addc_u32 s1, s43, s1
	v_lshl_add_u64 v[4:5], s[0:1], 0, v[2:3]
	s_mov_b64 s[0:1], 0
	s_mov_b64 s[2:3], 0x1000
